# conv_experts balance variant: 4 (not 3) tiles per job handed from workgroups 0..127 to w+128; plus exp1 preamble tables
# speedup vs baseline: 1.0051x; 1.0051x over previous
.LBB0_2820:
	s_add_i32 s43, s44, s93
	s_movk_i32 s32, 0xfff
	s_bitcmp0_b32 s92, 7
	s_cselect_b32 s32, 0xbff, s32
	s_cmp_gt_i32 s43, s32
	s_cbranch_scc0 .Lcbal0_go
	s_bitcmp1_b32 s44, 7
	s_cbranch_scc0 .Lcbal0_done
	s_add_i32 s43, s44, 0xfffffc80
	s_cmp_gt_i32 s43, 0xfff
	s_branch .Lcbal0_go

.LBB0_2834:
	s_add_i32 s41, s42, s93
	s_movk_i32 s32, 0xfff
	s_bitcmp0_b32 s92, 7
	s_cselect_b32 s32, 0xbff, s32
	s_cmp_gt_i32 s41, s32
	s_cbranch_scc0 .Lcbal2_go
	s_bitcmp1_b32 s42, 7
	s_cbranch_scc0 .Lcbal2_done
	s_add_i32 s41, s42, 0xfffffc80
	s_cmp_gt_i32 s41, 0xfff
	s_branch .Lcbal2_go
